# v3 + expert tile table not rebuilt in the down-GEMM and combine phases (still in LDS from the gate/up phase)
# speedup vs baseline: 1.0018x; 1.0018x over previous
; #define LAS __attribute__((address_space(3)))
; __device__ __forceinline__ void moe_build_table(Frame& F, int layer) {
;     LAS int* ts = (LAS int*)(F.lc + LC_TS); LAS int* cn = (LAS int*)(F.lc + LC_CNT);
;     __syncthreads();
;     if (F.wave == 0) {
;         const int c = (int)__hip_atomic_load(F.ctl + CW_CNT + layer * 64 + F.lane, RLX_AGENT);
;         int t = (c + 255) >> 8;
; #pragma unroll
;         for (int o = 1; o < 64; o <<= 1) { const int v = __shfl_up(t, o); if (F.lane >= o) t += v; }
;         cn[F.lane] = c; ts[F.lane + 1] = t;
;         if (F.lane == 0) ts[0] = 0;
;         if (F.lane == 63) ts[65] = t + 64;
;     }
;     __syncthreads();
; }
.LBB0_1682:
	s_cmp_le_i32 s92, s5
	s_cselect_b64 s[2:3], -1, 0
	s_and_b64 s[0:1], s[2:3], s[0:1]
	s_andn2_b64 vcc, exec, s[0:1]
	s_cbranch_vccnz .LBB0_1718
	v_readlane_b32 s40, v252, 2
	v_readfirstlane_b32 s5, v251
	v_and_b32_e32 v0, 63, v251
	v_readlane_b32 s41, v252, 3
	s_cmp_gt_u32 s5, 63
	s_waitcnt vmcnt(0) lgkmcnt(0)
	s_barrier
	s_branch .LBB0_1691
	s_lshl_b32 s22, s76, 6
	s_lshl_b64 s[2:3], s[22:23], 2
	v_readlane_b32 s6, v253, 38
	v_readlane_b32 s7, v253, 39
	s_add_u32 s2, s6, s2
	s_addc_u32 s3, s7, s3
	v_lshlrev_b32_e32 v2, 2, v0
	global_load_dword v4, v2, s[2:3] sc1
	v_and_b32_e32 v5, 64, v225
	v_add_u32_e32 v6, -1, v225
	v_cmp_lt_i32_e32 vcc, v6, v5
	v_readlane_b32 s2, v254, 45
	s_waitcnt vmcnt(0)
	v_add_u32_e32 v1, 0xff, v4
	v_cndmask_b32_e32 v6, v6, v225, vcc
	v_ashrrev_i32_e32 v1, 8, v1
	v_lshlrev_b32_e32 v6, 2, v6
	ds_bpermute_b32 v6, v6, v1
	v_cmp_ne_u32_e32 vcc, 0, v0
	s_waitcnt lgkmcnt(0)
	s_nop 0
	v_cndmask_b32_e32 v6, 0, v6, vcc
	v_add_u32_e32 v1, v6, v1
	v_add_u32_e32 v6, -2, v225
	v_cmp_lt_i32_e32 vcc, v6, v5
	s_nop 1
	v_cndmask_b32_e32 v6, v6, v225, vcc
	v_lshlrev_b32_e32 v6, 2, v6
	ds_bpermute_b32 v6, v6, v1
	v_cmp_lt_u32_e32 vcc, 1, v0
	s_waitcnt lgkmcnt(0)
	s_nop 0
	v_cndmask_b32_e32 v6, 0, v6, vcc
	v_add_u32_e32 v1, v6, v1
	v_add_u32_e32 v6, -4, v225
	v_cmp_lt_i32_e32 vcc, v6, v5
	s_nop 1
	v_cndmask_b32_e32 v6, v6, v225, vcc
	v_lshlrev_b32_e32 v6, 2, v6
	ds_bpermute_b32 v6, v6, v1
	v_cmp_lt_u32_e32 vcc, 3, v0
	s_waitcnt lgkmcnt(0)
	s_nop 0
	v_cndmask_b32_e32 v6, 0, v6, vcc
	v_add_u32_e32 v1, v6, v1
	v_add_u32_e32 v6, -8, v225
	v_cmp_lt_i32_e32 vcc, v6, v5
	s_nop 1
	v_cndmask_b32_e32 v6, v6, v225, vcc
	v_lshlrev_b32_e32 v6, 2, v6
	ds_bpermute_b32 v6, v6, v1
	v_cmp_lt_u32_e32 vcc, 7, v0
	s_waitcnt lgkmcnt(0)
	s_nop 0
	v_cndmask_b32_e32 v6, 0, v6, vcc
	v_add_u32_e32 v1, v6, v1
	v_add_u32_e32 v6, -16, v225
	v_cmp_lt_i32_e32 vcc, v6, v5
	s_nop 1
	v_cndmask_b32_e32 v6, v6, v225, vcc
	v_lshlrev_b32_e32 v6, 2, v6
	ds_bpermute_b32 v6, v6, v1
	v_cmp_lt_u32_e32 vcc, 15, v0
	s_waitcnt lgkmcnt(0)
	s_nop 0
	v_cndmask_b32_e32 v6, 0, v6, vcc
	v_add_u32_e32 v1, v6, v1
	v_subrev_u32_e32 v6, 32, v225
	v_cmp_lt_i32_e32 vcc, v6, v5
	s_nop 1
	v_cndmask_b32_e32 v5, v6, v225, vcc
	v_lshlrev_b32_e32 v5, 2, v5
	ds_bpermute_b32 v5, v5, v1
	v_cmp_lt_u32_e32 vcc, 31, v0
	s_waitcnt lgkmcnt(0)
	s_nop 0
	v_cndmask_b32_e32 v5, 0, v5, vcc
	v_add_u32_e32 v1, v5, v1
	v_add_u32_e32 v5, 0, v2
	v_add_u32_e32 v5, 0x21190, v5
	v_add_u32_e32 v2, s2, v2
	v_cmp_lt_i32_e32 vcc, 62, v0
	ds_write_b32 v5, v4
	ds_write_b32 v2, v1 offset:4
	s_and_saveexec_b64 s[2:3], vcc
	s_xor_b64 s[2:3], exec, s[2:3]
	s_cbranch_execz .LBB0_1686
	v_readlane_b32 s6, v254, 46
	v_add_u32_e32 v1, 64, v1
	s_nop 0
	v_mov_b32_e32 v2, s6
	ds_write_b32 v2, v1

; #define LAS __attribute__((address_space(3)))
; __device__ __forceinline__ void moe_build_table(Frame& F, int layer) {
;     LAS int* ts = (LAS int*)(F.lc + LC_TS); LAS int* cn = (LAS int*)(F.lc + LC_CNT);
;     __syncthreads();
;     if (F.wave == 0) {
;         const int c = (int)__hip_atomic_load(F.ctl + CW_CNT + layer * 64 + F.lane, RLX_AGENT);
;         int t = (c + 255) >> 8;
; #pragma unroll
;         for (int o = 1; o < 64; o <<= 1) { const int v = __shfl_up(t, o); if (F.lane >= o) t += v; }
;         cn[F.lane] = c; ts[F.lane + 1] = t;
;         if (F.lane == 0) ts[0] = 0;
;         if (F.lane == 63) ts[65] = t + 64;
;     }
;     __syncthreads();
; }
.LBB0_1772:
	s_cmp_le_i32 s92, s5
	s_cselect_b64 s[42:43], -1, 0
	s_and_b64 s[0:1], s[42:43], s[2:3]
	s_andn2_b64 vcc, exec, s[0:1]
	s_cbranch_vccnz .LBB0_1815
	v_mov_b32_e32 v0, v251
	v_readlane_b32 s0, v252, 2
	v_readfirstlane_b32 s5, v0
	s_waitcnt vmcnt(0)
	v_and_b32_e32 v28, 63, v0
	v_readlane_b32 s1, v252, 3
	s_cmp_gt_u32 s5, 63
	s_waitcnt lgkmcnt(0)
	s_barrier
	s_branch .LBB0_1781
	s_lshl_b32 s22, s76, 6
	s_lshl_b64 s[0:1], s[22:23], 2
	v_readlane_b32 s6, v253, 38
	v_readlane_b32 s7, v253, 39
	s_add_u32 s0, s6, s0
	s_addc_u32 s1, s7, s1
	v_lshlrev_b32_e32 v2, 2, v28
	global_load_dword v4, v2, s[0:1] sc1
	v_and_b32_e32 v5, 64, v225
	v_add_u32_e32 v6, -1, v225
	v_cmp_lt_i32_e32 vcc, v6, v5
	v_readlane_b32 s0, v254, 45
	s_waitcnt vmcnt(0)
	v_add_u32_e32 v1, 0xff, v4
	v_cndmask_b32_e32 v6, v6, v225, vcc
	v_ashrrev_i32_e32 v1, 8, v1
	v_lshlrev_b32_e32 v6, 2, v6
	ds_bpermute_b32 v6, v6, v1
	v_cmp_ne_u32_e32 vcc, 0, v28
	s_waitcnt lgkmcnt(0)
	s_nop 0
	v_cndmask_b32_e32 v6, 0, v6, vcc
	v_add_u32_e32 v1, v6, v1
	v_add_u32_e32 v6, -2, v225
	v_cmp_lt_i32_e32 vcc, v6, v5
	s_nop 1
	v_cndmask_b32_e32 v6, v6, v225, vcc
	v_lshlrev_b32_e32 v6, 2, v6
	ds_bpermute_b32 v6, v6, v1
	v_cmp_lt_u32_e32 vcc, 1, v28
	s_waitcnt lgkmcnt(0)
	s_nop 0
	v_cndmask_b32_e32 v6, 0, v6, vcc
	v_add_u32_e32 v1, v6, v1
	v_add_u32_e32 v6, -4, v225
	v_cmp_lt_i32_e32 vcc, v6, v5
	s_nop 1
	v_cndmask_b32_e32 v6, v6, v225, vcc
	v_lshlrev_b32_e32 v6, 2, v6
	ds_bpermute_b32 v6, v6, v1
	v_cmp_lt_u32_e32 vcc, 3, v28
	s_waitcnt lgkmcnt(0)
	s_nop 0
	v_cndmask_b32_e32 v6, 0, v6, vcc
	v_add_u32_e32 v1, v6, v1
	v_add_u32_e32 v6, -8, v225
	v_cmp_lt_i32_e32 vcc, v6, v5
	s_nop 1
	v_cndmask_b32_e32 v6, v6, v225, vcc
	v_lshlrev_b32_e32 v6, 2, v6
	ds_bpermute_b32 v6, v6, v1
	v_cmp_lt_u32_e32 vcc, 7, v28
	s_waitcnt lgkmcnt(0)
	s_nop 0
	v_cndmask_b32_e32 v6, 0, v6, vcc
	v_add_u32_e32 v1, v6, v1
	v_add_u32_e32 v6, -16, v225
	v_cmp_lt_i32_e32 vcc, v6, v5
	s_nop 1
	v_cndmask_b32_e32 v6, v6, v225, vcc
	v_lshlrev_b32_e32 v6, 2, v6
	ds_bpermute_b32 v6, v6, v1
	v_cmp_lt_u32_e32 vcc, 15, v28
	s_waitcnt lgkmcnt(0)
	s_nop 0
	v_cndmask_b32_e32 v6, 0, v6, vcc
	v_add_u32_e32 v1, v6, v1
	v_subrev_u32_e32 v6, 32, v225
	v_cmp_lt_i32_e32 vcc, v6, v5
	s_nop 1
	v_cndmask_b32_e32 v5, v6, v225, vcc
	v_lshlrev_b32_e32 v5, 2, v5
	ds_bpermute_b32 v5, v5, v1
	v_cmp_lt_u32_e32 vcc, 31, v28
	s_waitcnt lgkmcnt(0)
	s_nop 0
	v_cndmask_b32_e32 v5, 0, v5, vcc
	v_add_u32_e32 v1, v5, v1
	v_add_u32_e32 v5, 0, v2
	v_add_u32_e32 v5, 0x21190, v5
	v_add_u32_e32 v2, s0, v2
	v_cmp_lt_i32_e32 vcc, 62, v28
	ds_write_b32 v5, v4
	ds_write_b32 v2, v1 offset:4
	s_and_saveexec_b64 s[0:1], vcc
	s_xor_b64 s[0:1], exec, s[0:1]
	s_cbranch_execz .LBB0_1776
	v_readlane_b32 s6, v254, 46
	v_add_u32_e32 v1, 64, v1
	s_nop 0
	v_mov_b32_e32 v2, s6
	ds_write_b32 v2, v1
